# speedup vs baseline: 1.1537x; 1.0358x over previous
_Z11center_mainPKfPKcS0_Pf:
	s_load_dwordx4 s[4:7], s[0:1], 0x0
	s_load_dwordx2 s[8:9], s[0:1], 0x10
	s_and_b32 s3, s2, 7
	s_lshr_b32 s12, s2, 3
	s_mov_b32 s30, s2
	v_lshrrev_b32_e32 v1, 6, v0
	v_and_b32_e32 v2, 63, v0
	v_bfe_u32 v3, v0, 3, 3
	v_and_b32_e32 v4, 7, v0
	v_lshrrev_b32_e32 v5, 7, v0
	v_bfe_u32 v6, v0, 6, 1
	v_lshl_or_b32 v7, v5, 3, v3
	v_lshlrev_b32_e32 v8, 10, v7
	v_lshl_or_b32 v8, v6, 9, v8
	v_lshl_or_b32 v226, v4, 4, v8
	v_lshlrev_b32_e32 v17, 15, v1
	v_lshl_or_b32 v227, v2, 5, v17
	v_lshlrev_b32_e32 v237, 3, v0
	s_lshl_b32 s13, s3, 22
	s_lshl_b32 s14, s12, 15
	s_add_u32 s13, s13, s14
	s_lshl_b32 s15, s3, 18
	s_lshl_b32 s28, s3, 12
	s_waitcnt lgkmcnt(0)
	s_add_u32 s16, s4, s13
	s_addc_u32 s17, s5, 0
	global_load_dwordx4 v[194:197], v226, s[16:17] offset:0 nt
	global_load_dwordx4 v[198:201], v226, s[16:17] offset:128 nt
	global_load_dwordx4 v[202:205], v226, s[16:17] offset:256 nt
	global_load_dwordx4 v[206:209], v226, s[16:17] offset:384 nt
	s_add_u32 s8, s8, s28
	s_addc_u32 s9, s9, 0
	global_load_dwordx2 v[238:239], v237, s[8:9]
	s_add_u32 s24, s6, s15
	s_addc_u32 s25, s7, 0
	s_add_u32 s32, s24, 0x1000
	s_addc_u32 s33, s25, 0
	s_add_u32 s34, s24, 0x2000
	s_addc_u32 s35, s25, 0
	s_add_u32 s36, s24, 0x3000
	s_addc_u32 s37, s25, 0
	s_add_u32 s38, s24, 0x4000
	s_addc_u32 s39, s25, 0
	s_add_u32 s40, s24, 0x5000
	s_addc_u32 s41, s25, 0
	s_add_u32 s42, s24, 0x6000
	s_addc_u32 s43, s25, 0
	s_add_u32 s44, s24, 0x7000
	s_addc_u32 s45, s25, 0
	global_load_dwordx4 v[34:37], v227, s[24:25] offset:0
	global_load_dwordx4 v[38:41], v227, s[24:25] offset:16
	global_load_dwordx4 v[26:29], v227, s[24:25] offset:2048
	global_load_dwordx4 v[30:33], v227, s[24:25] offset:2064
	global_load_dwordx4 v[50:53], v227, s[32:33] offset:0
	global_load_dwordx4 v[54:57], v227, s[32:33] offset:16
	global_load_dwordx4 v[42:45], v227, s[32:33] offset:2048
	global_load_dwordx4 v[46:49], v227, s[32:33] offset:2064
	global_load_dwordx4 v[18:21], v227, s[34:35] offset:0
	global_load_dwordx4 v[22:25], v227, s[34:35] offset:16
	global_load_dwordx4 v[130:133], v227, s[34:35] offset:2048
	global_load_dwordx4 v[134:137], v227, s[34:35] offset:2064
	global_load_dwordx4 v[122:125], v227, s[36:37] offset:0
	global_load_dwordx4 v[126:129], v227, s[36:37] offset:16
	global_load_dwordx4 v[138:141], v227, s[36:37] offset:2048
	global_load_dwordx4 v[142:145], v227, s[36:37] offset:2064
	global_load_dwordx4 v[98:101], v227, s[38:39] offset:0
	global_load_dwordx4 v[102:105], v227, s[38:39] offset:16
	global_load_dwordx4 v[90:93], v227, s[38:39] offset:2048
	global_load_dwordx4 v[94:97], v227, s[38:39] offset:2064
	global_load_dwordx4 v[114:117], v227, s[40:41] offset:0
	global_load_dwordx4 v[118:121], v227, s[40:41] offset:16
	global_load_dwordx4 v[106:109], v227, s[40:41] offset:2048
	global_load_dwordx4 v[110:113], v227, s[40:41] offset:2064
	global_load_dwordx4 v[58:61], v227, s[42:43] offset:0
	global_load_dwordx4 v[62:65], v227, s[42:43] offset:16
	global_load_dwordx4 v[66:69], v227, s[42:43] offset:2048
	global_load_dwordx4 v[70:73], v227, s[42:43] offset:2064
	global_load_dwordx4 v[74:77], v227, s[44:45] offset:0
	global_load_dwordx4 v[78:81], v227, s[44:45] offset:16
	global_load_dwordx4 v[82:85], v227, s[44:45] offset:2048
	global_load_dwordx4 v[86:89], v227, s[44:45] offset:2064
	s_add_u32 s18, s16, 0x100000
	s_addc_u32 s19, s17, 0
	s_add_u32 s20, s16, 0x200000
	s_addc_u32 s21, s17, 0
	s_add_u32 s22, s16, 0x300000
	s_addc_u32 s23, s17, 0
	v_mul_u32_u24_e32 v9, 0x110, v7
	v_lshl_add_u32 v9, v6, 7, v9
	v_lshl_add_u32 v228, v4, 4, v9
	v_lshlrev_b32_e32 v10, 6, v7
	v_lshl_or_b32 v10, v6, 5, v10
	v_lshl_or_b32 v229, v4, 2, v10
	v_and_b32_e32 v11, 31, v0
	v_bfe_u32 v12, v0, 5, 1
	v_mul_u32_u24_e32 v13, 0x110, v11
	v_lshl_add_u32 v230, v12, 5, v13
	v_lshlrev_b32_e32 v14, 9, v1
	v_lshl_or_b32 v231, v12, 4, v14
	v_xor_b32_e32 v15, 32, v2
	v_lshlrev_b32_e32 v232, 2, v15
	v_xor_b32_e32 v15, 16, v2
	v_lshlrev_b32_e32 v247, 2, v15
	v_lshlrev_b32_e32 v16, 7, v1
	v_lshl_or_b32 v233, v11, 2, v16
	v_mov_b32_e32 v234, 0x7f7f7f7f
	s_waitcnt vmcnt(32)
	ds_write_b64 v237, v[238:239] offset:34816
	v_mul_f32_e32 v244, v194, v194
	v_mul_f32_e32 v245, v198, v198
	v_cvt_pk_fp8_f32 v240, v194, v195
	v_cvt_pk_fp8_f32 v241, v198, v199
	v_cvt_pk_fp8_f32 v242, v202, v203
	v_cvt_pk_fp8_f32 v243, v206, v207
	v_fmac_f32_e32 v244, v195, v195
	v_fmac_f32_e32 v245, v199, v199
	v_fmac_f32_e32 v244, v196, v196
	v_fmac_f32_e32 v245, v200, v200
	v_fmac_f32_e32 v244, v197, v197
	v_fmac_f32_e32 v245, v201, v201
	v_fmac_f32_e32 v244, v202, v202
	v_fmac_f32_e32 v245, v206, v206
	v_fmac_f32_e32 v244, v203, v203
	v_fmac_f32_e32 v245, v207, v207
	v_fmac_f32_e32 v244, v204, v204
	v_fmac_f32_e32 v245, v208, v208
	v_fmac_f32_e32 v244, v205, v205
	v_fmac_f32_e32 v245, v209, v209
	v_cvt_pk_fp8_f32 v240, v196, v197 op_sel:[0,0,1]
	v_cvt_pk_fp8_f32 v241, v200, v201 op_sel:[0,0,1]
	v_cvt_pk_fp8_f32 v242, v204, v205 op_sel:[0,0,1]
	v_cvt_pk_fp8_f32 v243, v208, v209 op_sel:[0,0,1]
	v_add_f32_e32 v244, v244, v245
	s_nop 0
	ds_write_b128 v228, v[240:243] offset:0
	ds_write_b32 v229, v244 offset:38912
	global_load_dwordx4 v[210:213], v226, s[18:19] offset:0 nt
	global_load_dwordx4 v[214:217], v226, s[18:19] offset:128 nt
	global_load_dwordx4 v[218:221], v226, s[18:19] offset:256 nt
	global_load_dwordx4 v[222:225], v226, s[18:19] offset:384 nt
	s_waitcnt lgkmcnt(0)
	s_barrier
	ds_read_b128 v[162:165], v230 offset:0
	ds_read_b128 v[166:169], v230 offset:16
	ds_read_b128 v[2:5], v231 offset:34816
	ds_read_b128 v[6:9], v231 offset:34848
	ds_read_b128 v[10:13], v231 offset:34880
	ds_read_b128 v[14:17], v231 offset:34912
	ds_read_b128 v[170:173], v230 offset:64
	ds_read_b128 v[174:177], v230 offset:80
	ds_read_b128 v[178:181], v230 offset:128
	ds_read_b128 v[182:185], v230 offset:144
	ds_read_b128 v[186:189], v230 offset:192
	ds_read_b128 v[190:193], v230 offset:208
	s_waitcnt vmcnt(34) lgkmcnt(6)
	v_mfma_scale_f32_32x32x64_f8f6f4 v[2:17], v[34:41], v[162:169], v[2:17], v234, v234 op_sel_hi:[0,0,0]
	s_waitcnt vmcnt(32) lgkmcnt(4)
	v_mfma_scale_f32_32x32x64_f8f6f4 v[2:17], v[26:33], v[170:177], v[2:17], v234, v234 op_sel_hi:[0,0,0]
	s_waitcnt vmcnt(30) lgkmcnt(2)
	v_mfma_scale_f32_32x32x64_f8f6f4 v[2:17], v[50:57], v[178:185], v[2:17], v234, v234 op_sel_hi:[0,0,0]
	s_waitcnt vmcnt(28) lgkmcnt(0)
	v_mfma_scale_f32_32x32x64_f8f6f4 v[2:17], v[42:49], v[186:193], v[2:17], v234, v234 op_sel_hi:[0,0,0]
	ds_read_b128 v[146:149], v231 offset:34944
	ds_read_b128 v[150:153], v231 offset:34976
	ds_read_b128 v[154:157], v231 offset:35008
	ds_read_b128 v[158:161], v231 offset:35040
	s_waitcnt vmcnt(26) lgkmcnt(0)
	v_mfma_scale_f32_32x32x64_f8f6f4 v[146:161], v[18:25], v[162:169], v[146:161], v234, v234 op_sel_hi:[0,0,0]
	s_waitcnt vmcnt(24)
	v_mfma_scale_f32_32x32x64_f8f6f4 v[146:161], v[130:137], v[170:177], v[146:161], v234, v234 op_sel_hi:[0,0,0]
	s_waitcnt vmcnt(22)
	v_mfma_scale_f32_32x32x64_f8f6f4 v[146:161], v[122:129], v[178:185], v[146:161], v234, v234 op_sel_hi:[0,0,0]
	s_waitcnt vmcnt(20)
	v_mfma_scale_f32_32x32x64_f8f6f4 v[146:161], v[138:145], v[186:193], v[146:161], v234, v234 op_sel_hi:[0,0,0]
	s_nop 15
	v_min3_f32 v2, v2, v3, v4
	v_min3_f32 v5, v5, v6, v7
	v_min3_f32 v8, v8, v9, v10
	v_min3_f32 v11, v11, v12, v13
	v_min3_f32 v14, v14, v15, v16
	v_min3_f32 v2, v2, v5, v8
	v_min3_f32 v11, v11, v14, v17
	v_min_f32_e32 v235, v2, v11
	ds_read_b128 v[2:5], v231 offset:35072
	ds_read_b128 v[6:9], v231 offset:35104
	ds_read_b128 v[10:13], v231 offset:35136
	ds_read_b128 v[14:17], v231 offset:35168
	s_waitcnt vmcnt(18) lgkmcnt(0)
	v_mfma_scale_f32_32x32x64_f8f6f4 v[2:17], v[98:105], v[162:169], v[2:17], v234, v234 op_sel_hi:[0,0,0]
	s_waitcnt vmcnt(16)
	v_mfma_scale_f32_32x32x64_f8f6f4 v[2:17], v[90:97], v[170:177], v[2:17], v234, v234 op_sel_hi:[0,0,0]
	s_waitcnt vmcnt(14)
	v_mfma_scale_f32_32x32x64_f8f6f4 v[2:17], v[114:121], v[178:185], v[2:17], v234, v234 op_sel_hi:[0,0,0]
	s_waitcnt vmcnt(12)
	v_mfma_scale_f32_32x32x64_f8f6f4 v[2:17], v[106:113], v[186:193], v[2:17], v234, v234 op_sel_hi:[0,0,0]
	s_nop 15
	v_min3_f32 v146, v146, v147, v148
	v_min3_f32 v149, v149, v150, v151
	v_min3_f32 v152, v152, v153, v154
	v_min3_f32 v155, v155, v156, v157
	v_min3_f32 v158, v158, v159, v160
	v_min3_f32 v146, v146, v149, v152
	v_min3_f32 v155, v155, v158, v161
	v_min3_f32 v235, v235, v146, v155
	ds_read_b128 v[146:149], v231 offset:35200
	ds_read_b128 v[150:153], v231 offset:35232
	ds_read_b128 v[154:157], v231 offset:35264
	ds_read_b128 v[158:161], v231 offset:35296
	s_waitcnt vmcnt(10) lgkmcnt(0)
	v_mfma_scale_f32_32x32x64_f8f6f4 v[146:161], v[58:65], v[162:169], v[146:161], v234, v234 op_sel_hi:[0,0,0]
	s_waitcnt vmcnt(8)
	v_mfma_scale_f32_32x32x64_f8f6f4 v[146:161], v[66:73], v[170:177], v[146:161], v234, v234 op_sel_hi:[0,0,0]
	s_waitcnt vmcnt(6)
	v_mfma_scale_f32_32x32x64_f8f6f4 v[146:161], v[74:81], v[178:185], v[146:161], v234, v234 op_sel_hi:[0,0,0]
	s_waitcnt vmcnt(4)
	v_mfma_scale_f32_32x32x64_f8f6f4 v[146:161], v[82:89], v[186:193], v[146:161], v234, v234 op_sel_hi:[0,0,0]
	global_load_dwordx4 v[194:197], v226, s[20:21] offset:0 nt
	global_load_dwordx4 v[198:201], v226, s[20:21] offset:128 nt
	global_load_dwordx4 v[202:205], v226, s[20:21] offset:256 nt
	global_load_dwordx4 v[206:209], v226, s[20:21] offset:384 nt
	s_waitcnt vmcnt(4)
	v_mul_f32_e32 v244, v210, v210
	v_mul_f32_e32 v245, v214, v214
	v_cvt_pk_fp8_f32 v240, v210, v211
	v_cvt_pk_fp8_f32 v241, v214, v215
	v_cvt_pk_fp8_f32 v242, v218, v219
	v_cvt_pk_fp8_f32 v243, v222, v223
	v_fmac_f32_e32 v244, v211, v211
	v_fmac_f32_e32 v245, v215, v215
	v_fmac_f32_e32 v244, v212, v212
	v_fmac_f32_e32 v245, v216, v216
	v_fmac_f32_e32 v244, v213, v213
	v_fmac_f32_e32 v245, v217, v217
	v_fmac_f32_e32 v244, v218, v218
	v_fmac_f32_e32 v245, v222, v222
	v_fmac_f32_e32 v244, v219, v219
	v_fmac_f32_e32 v245, v223, v223
	v_fmac_f32_e32 v244, v220, v220
	v_fmac_f32_e32 v245, v224, v224
	v_fmac_f32_e32 v244, v221, v221
	v_fmac_f32_e32 v245, v225, v225
	v_cvt_pk_fp8_f32 v240, v212, v213 op_sel:[0,0,1]
	v_cvt_pk_fp8_f32 v241, v216, v217 op_sel:[0,0,1]
	v_cvt_pk_fp8_f32 v242, v220, v221 op_sel:[0,0,1]
	v_cvt_pk_fp8_f32 v243, v224, v225 op_sel:[0,0,1]
	v_add_f32_e32 v244, v244, v245
	s_nop 0
	ds_write_b128 v228, v[240:243] offset:8704
	ds_write_b32 v229, v244 offset:40960
	s_waitcnt lgkmcnt(0)
	s_barrier
	ds_read_b128 v[162:165], v230 offset:8704
	ds_read_b128 v[166:169], v230 offset:8720
	v_min3_f32 v2, v2, v3, v4
	v_min3_f32 v5, v5, v6, v7
	v_min3_f32 v8, v8, v9, v10
	v_min3_f32 v11, v11, v12, v13
	v_min3_f32 v14, v14, v15, v16
	v_min3_f32 v2, v2, v5, v8
	v_min3_f32 v11, v11, v14, v17
	v_min3_f32 v235, v235, v2, v11
	ds_read_b128 v[2:5], v231 offset:34816
	ds_read_b128 v[6:9], v231 offset:34848
	ds_read_b128 v[10:13], v231 offset:34880
	ds_read_b128 v[14:17], v231 offset:34912
	ds_read_b128 v[170:173], v230 offset:8768
	ds_read_b128 v[174:177], v230 offset:8784
	ds_read_b128 v[178:181], v230 offset:8832
	ds_read_b128 v[182:185], v230 offset:8848
	ds_read_b128 v[186:189], v230 offset:8896
	ds_read_b128 v[190:193], v230 offset:8912
	s_waitcnt lgkmcnt(6)
	v_mfma_scale_f32_32x32x64_f8f6f4 v[2:17], v[34:41], v[162:169], v[2:17], v234, v234 op_sel_hi:[0,0,0]
	s_waitcnt lgkmcnt(4)
	v_mfma_scale_f32_32x32x64_f8f6f4 v[2:17], v[26:33], v[170:177], v[2:17], v234, v234 op_sel_hi:[0,0,0]
	s_waitcnt lgkmcnt(2)
	v_mfma_scale_f32_32x32x64_f8f6f4 v[2:17], v[50:57], v[178:185], v[2:17], v234, v234 op_sel_hi:[0,0,0]
	s_waitcnt lgkmcnt(0)
	v_mfma_scale_f32_32x32x64_f8f6f4 v[2:17], v[42:49], v[186:193], v[2:17], v234, v234 op_sel_hi:[0,0,0]
	s_nop 15
	v_min3_f32 v146, v146, v147, v148
	v_min3_f32 v149, v149, v150, v151
	v_min3_f32 v152, v152, v153, v154
	v_min3_f32 v155, v155, v156, v157
	v_min3_f32 v158, v158, v159, v160
	v_min3_f32 v146, v146, v149, v152
	v_min3_f32 v155, v155, v158, v161
	v_min3_f32 v235, v235, v146, v155
	ds_bpermute_b32 v246, v232, v235
	s_waitcnt lgkmcnt(0)
	v_min_f32_e32 v246, v235, v246
	ds_write_b32 v233, v246 offset:47104
	ds_read_b128 v[146:149], v231 offset:34944
	ds_read_b128 v[150:153], v231 offset:34976
	ds_read_b128 v[154:157], v231 offset:35008
	ds_read_b128 v[158:161], v231 offset:35040
	s_waitcnt lgkmcnt(0)
	v_mfma_scale_f32_32x32x64_f8f6f4 v[146:161], v[18:25], v[162:169], v[146:161], v234, v234 op_sel_hi:[0,0,0]
	v_mfma_scale_f32_32x32x64_f8f6f4 v[146:161], v[130:137], v[170:177], v[146:161], v234, v234 op_sel_hi:[0,0,0]
	v_mfma_scale_f32_32x32x64_f8f6f4 v[146:161], v[122:129], v[178:185], v[146:161], v234, v234 op_sel_hi:[0,0,0]
	v_mfma_scale_f32_32x32x64_f8f6f4 v[146:161], v[138:145], v[186:193], v[146:161], v234, v234 op_sel_hi:[0,0,0]
	s_nop 15
	v_min3_f32 v2, v2, v3, v4
	v_min3_f32 v5, v5, v6, v7
	v_min3_f32 v8, v8, v9, v10
	v_min3_f32 v11, v11, v12, v13
	v_min3_f32 v14, v14, v15, v16
	v_min3_f32 v2, v2, v5, v8
	v_min3_f32 v11, v11, v14, v17
	v_min_f32_e32 v236, v2, v11
	ds_read_b128 v[2:5], v231 offset:35072
	ds_read_b128 v[6:9], v231 offset:35104
	ds_read_b128 v[10:13], v231 offset:35136
	ds_read_b128 v[14:17], v231 offset:35168
	s_waitcnt lgkmcnt(0)
	v_mfma_scale_f32_32x32x64_f8f6f4 v[2:17], v[98:105], v[162:169], v[2:17], v234, v234 op_sel_hi:[0,0,0]
	v_mfma_scale_f32_32x32x64_f8f6f4 v[2:17], v[90:97], v[170:177], v[2:17], v234, v234 op_sel_hi:[0,0,0]
	v_mfma_scale_f32_32x32x64_f8f6f4 v[2:17], v[114:121], v[178:185], v[2:17], v234, v234 op_sel_hi:[0,0,0]
	v_mfma_scale_f32_32x32x64_f8f6f4 v[2:17], v[106:113], v[186:193], v[2:17], v234, v234 op_sel_hi:[0,0,0]
	s_nop 15
	v_min3_f32 v146, v146, v147, v148
	v_min3_f32 v149, v149, v150, v151
	v_min3_f32 v152, v152, v153, v154
	v_min3_f32 v155, v155, v156, v157
	v_min3_f32 v158, v158, v159, v160
	v_min3_f32 v146, v146, v149, v152
	v_min3_f32 v155, v155, v158, v161
	v_min3_f32 v236, v236, v146, v155
	ds_read_b128 v[146:149], v231 offset:35200
	ds_read_b128 v[150:153], v231 offset:35232
	ds_read_b128 v[154:157], v231 offset:35264
	ds_read_b128 v[158:161], v231 offset:35296
	s_waitcnt lgkmcnt(0)
	v_mfma_scale_f32_32x32x64_f8f6f4 v[146:161], v[58:65], v[162:169], v[146:161], v234, v234 op_sel_hi:[0,0,0]
	v_mfma_scale_f32_32x32x64_f8f6f4 v[146:161], v[66:73], v[170:177], v[146:161], v234, v234 op_sel_hi:[0,0,0]
	v_mfma_scale_f32_32x32x64_f8f6f4 v[146:161], v[74:81], v[178:185], v[146:161], v234, v234 op_sel_hi:[0,0,0]
	v_mfma_scale_f32_32x32x64_f8f6f4 v[146:161], v[82:89], v[186:193], v[146:161], v234, v234 op_sel_hi:[0,0,0]
	global_load_dwordx4 v[210:213], v226, s[22:23] offset:0 nt
	global_load_dwordx4 v[214:217], v226, s[22:23] offset:128 nt
	global_load_dwordx4 v[218:221], v226, s[22:23] offset:256 nt
	global_load_dwordx4 v[222:225], v226, s[22:23] offset:384 nt
	s_waitcnt vmcnt(4)
	v_mul_f32_e32 v244, v194, v194
	v_mul_f32_e32 v245, v198, v198
	v_cvt_pk_fp8_f32 v240, v194, v195
	v_cvt_pk_fp8_f32 v241, v198, v199
	v_cvt_pk_fp8_f32 v242, v202, v203
	v_cvt_pk_fp8_f32 v243, v206, v207
	v_fmac_f32_e32 v244, v195, v195
	v_fmac_f32_e32 v245, v199, v199
	v_fmac_f32_e32 v244, v196, v196
	v_fmac_f32_e32 v245, v200, v200
	v_fmac_f32_e32 v244, v197, v197
	v_fmac_f32_e32 v245, v201, v201
	v_fmac_f32_e32 v244, v202, v202
	v_fmac_f32_e32 v245, v206, v206
	v_fmac_f32_e32 v244, v203, v203
	v_fmac_f32_e32 v245, v207, v207
	v_fmac_f32_e32 v244, v204, v204
	v_fmac_f32_e32 v245, v208, v208
	v_fmac_f32_e32 v244, v205, v205
	v_fmac_f32_e32 v245, v209, v209
	v_cvt_pk_fp8_f32 v240, v196, v197 op_sel:[0,0,1]
	v_cvt_pk_fp8_f32 v241, v200, v201 op_sel:[0,0,1]
	v_cvt_pk_fp8_f32 v242, v204, v205 op_sel:[0,0,1]
	v_cvt_pk_fp8_f32 v243, v208, v209 op_sel:[0,0,1]
	v_add_f32_e32 v244, v244, v245
	s_nop 0
	ds_write_b128 v228, v[240:243] offset:17408
	ds_write_b32 v229, v244 offset:43008
	s_waitcnt lgkmcnt(0)
	s_barrier
	ds_read_b128 v[162:165], v230 offset:17408
	ds_read_b128 v[166:169], v230 offset:17424
	v_min3_f32 v2, v2, v3, v4
	v_min3_f32 v5, v5, v6, v7
	v_min3_f32 v8, v8, v9, v10
	v_min3_f32 v11, v11, v12, v13
	v_min3_f32 v14, v14, v15, v16
	v_min3_f32 v2, v2, v5, v8
	v_min3_f32 v11, v11, v14, v17
	v_min3_f32 v236, v236, v2, v11
	ds_read_b128 v[2:5], v231 offset:34816
	ds_read_b128 v[6:9], v231 offset:34848
	ds_read_b128 v[10:13], v231 offset:34880
	ds_read_b128 v[14:17], v231 offset:34912
	ds_read_b128 v[170:173], v230 offset:17472
	ds_read_b128 v[174:177], v230 offset:17488
	ds_read_b128 v[178:181], v230 offset:17536
	ds_read_b128 v[182:185], v230 offset:17552
	ds_read_b128 v[186:189], v230 offset:17600
	ds_read_b128 v[190:193], v230 offset:17616
	s_waitcnt lgkmcnt(6)
	v_mfma_scale_f32_32x32x64_f8f6f4 v[2:17], v[34:41], v[162:169], v[2:17], v234, v234 op_sel_hi:[0,0,0]
	s_waitcnt lgkmcnt(4)
	v_mfma_scale_f32_32x32x64_f8f6f4 v[2:17], v[26:33], v[170:177], v[2:17], v234, v234 op_sel_hi:[0,0,0]
	s_waitcnt lgkmcnt(2)
	v_mfma_scale_f32_32x32x64_f8f6f4 v[2:17], v[50:57], v[178:185], v[2:17], v234, v234 op_sel_hi:[0,0,0]
	s_waitcnt lgkmcnt(0)
	v_mfma_scale_f32_32x32x64_f8f6f4 v[2:17], v[42:49], v[186:193], v[2:17], v234, v234 op_sel_hi:[0,0,0]
	s_nop 15
	v_min3_f32 v146, v146, v147, v148
	v_min3_f32 v149, v149, v150, v151
	v_min3_f32 v152, v152, v153, v154
	v_min3_f32 v155, v155, v156, v157
	v_min3_f32 v158, v158, v159, v160
	v_min3_f32 v146, v146, v149, v152
	v_min3_f32 v155, v155, v158, v161
	v_min3_f32 v236, v236, v146, v155
	ds_bpermute_b32 v246, v232, v236
	s_waitcnt lgkmcnt(0)
	v_min_f32_e32 v246, v236, v246
	ds_write_b32 v233, v246 offset:48128
	ds_read_b128 v[146:149], v231 offset:34944
	ds_read_b128 v[150:153], v231 offset:34976
	ds_read_b128 v[154:157], v231 offset:35008
	ds_read_b128 v[158:161], v231 offset:35040
	s_waitcnt lgkmcnt(0)
	v_mfma_scale_f32_32x32x64_f8f6f4 v[146:161], v[18:25], v[162:169], v[146:161], v234, v234 op_sel_hi:[0,0,0]
	v_mfma_scale_f32_32x32x64_f8f6f4 v[146:161], v[130:137], v[170:177], v[146:161], v234, v234 op_sel_hi:[0,0,0]
	v_mfma_scale_f32_32x32x64_f8f6f4 v[146:161], v[122:129], v[178:185], v[146:161], v234, v234 op_sel_hi:[0,0,0]
	v_mfma_scale_f32_32x32x64_f8f6f4 v[146:161], v[138:145], v[186:193], v[146:161], v234, v234 op_sel_hi:[0,0,0]
	s_nop 15
	v_min3_f32 v2, v2, v3, v4
	v_min3_f32 v5, v5, v6, v7
	v_min3_f32 v8, v8, v9, v10
	v_min3_f32 v11, v11, v12, v13
	v_min3_f32 v14, v14, v15, v16
	v_min3_f32 v2, v2, v5, v8
	v_min3_f32 v11, v11, v14, v17
	v_min_f32_e32 v235, v2, v11
	ds_read_b128 v[2:5], v231 offset:35072
	ds_read_b128 v[6:9], v231 offset:35104
	ds_read_b128 v[10:13], v231 offset:35136
	ds_read_b128 v[14:17], v231 offset:35168
	s_waitcnt lgkmcnt(0)
	v_mfma_scale_f32_32x32x64_f8f6f4 v[2:17], v[98:105], v[162:169], v[2:17], v234, v234 op_sel_hi:[0,0,0]
	v_mfma_scale_f32_32x32x64_f8f6f4 v[2:17], v[90:97], v[170:177], v[2:17], v234, v234 op_sel_hi:[0,0,0]
	v_mfma_scale_f32_32x32x64_f8f6f4 v[2:17], v[114:121], v[178:185], v[2:17], v234, v234 op_sel_hi:[0,0,0]
	v_mfma_scale_f32_32x32x64_f8f6f4 v[2:17], v[106:113], v[186:193], v[2:17], v234, v234 op_sel_hi:[0,0,0]
	s_nop 15
	v_min3_f32 v146, v146, v147, v148
	v_min3_f32 v149, v149, v150, v151
	v_min3_f32 v152, v152, v153, v154
	v_min3_f32 v155, v155, v156, v157
	v_min3_f32 v158, v158, v159, v160
	v_min3_f32 v146, v146, v149, v152
	v_min3_f32 v155, v155, v158, v161
	v_min3_f32 v235, v235, v146, v155
	ds_read_b128 v[146:149], v231 offset:35200
	ds_read_b128 v[150:153], v231 offset:35232
	ds_read_b128 v[154:157], v231 offset:35264
	ds_read_b128 v[158:161], v231 offset:35296
	s_waitcnt lgkmcnt(0)
	v_mfma_scale_f32_32x32x64_f8f6f4 v[146:161], v[58:65], v[162:169], v[146:161], v234, v234 op_sel_hi:[0,0,0]
	v_mfma_scale_f32_32x32x64_f8f6f4 v[146:161], v[66:73], v[170:177], v[146:161], v234, v234 op_sel_hi:[0,0,0]
	v_mfma_scale_f32_32x32x64_f8f6f4 v[146:161], v[74:81], v[178:185], v[146:161], v234, v234 op_sel_hi:[0,0,0]
	v_mfma_scale_f32_32x32x64_f8f6f4 v[146:161], v[82:89], v[186:193], v[146:161], v234, v234 op_sel_hi:[0,0,0]
	s_waitcnt vmcnt(0)
	v_mul_f32_e32 v244, v210, v210
	v_mul_f32_e32 v245, v214, v214
	v_cvt_pk_fp8_f32 v240, v210, v211
	v_cvt_pk_fp8_f32 v241, v214, v215
	v_cvt_pk_fp8_f32 v242, v218, v219
	v_cvt_pk_fp8_f32 v243, v222, v223
	v_fmac_f32_e32 v244, v211, v211
	v_fmac_f32_e32 v245, v215, v215
	v_fmac_f32_e32 v244, v212, v212
	v_fmac_f32_e32 v245, v216, v216
	v_fmac_f32_e32 v244, v213, v213
	v_fmac_f32_e32 v245, v217, v217
	v_fmac_f32_e32 v244, v218, v218
	v_fmac_f32_e32 v245, v222, v222
	v_fmac_f32_e32 v244, v219, v219
	v_fmac_f32_e32 v245, v223, v223
	v_fmac_f32_e32 v244, v220, v220
	v_fmac_f32_e32 v245, v224, v224
	v_fmac_f32_e32 v244, v221, v221
	v_fmac_f32_e32 v245, v225, v225
	v_cvt_pk_fp8_f32 v240, v212, v213 op_sel:[0,0,1]
	v_cvt_pk_fp8_f32 v241, v216, v217 op_sel:[0,0,1]
	v_cvt_pk_fp8_f32 v242, v220, v221 op_sel:[0,0,1]
	v_cvt_pk_fp8_f32 v243, v224, v225 op_sel:[0,0,1]
	v_add_f32_e32 v244, v244, v245
	s_nop 0
	ds_write_b128 v228, v[240:243] offset:26112
	ds_write_b32 v229, v244 offset:45056
	s_waitcnt lgkmcnt(0)
	s_barrier
	ds_read_b128 v[162:165], v230 offset:26112
	ds_read_b128 v[166:169], v230 offset:26128
	v_min3_f32 v2, v2, v3, v4
	v_min3_f32 v5, v5, v6, v7
	v_min3_f32 v8, v8, v9, v10
	v_min3_f32 v11, v11, v12, v13
	v_min3_f32 v14, v14, v15, v16
	v_min3_f32 v2, v2, v5, v8
	v_min3_f32 v11, v11, v14, v17
	v_min3_f32 v235, v235, v2, v11
	ds_read_b128 v[2:5], v231 offset:34816
	ds_read_b128 v[6:9], v231 offset:34848
	ds_read_b128 v[10:13], v231 offset:34880
	ds_read_b128 v[14:17], v231 offset:34912
	ds_read_b128 v[170:173], v230 offset:26176
	ds_read_b128 v[174:177], v230 offset:26192
	ds_read_b128 v[178:181], v230 offset:26240
	ds_read_b128 v[182:185], v230 offset:26256
	ds_read_b128 v[186:189], v230 offset:26304
	ds_read_b128 v[190:193], v230 offset:26320
	s_waitcnt lgkmcnt(6)
	v_mfma_scale_f32_32x32x64_f8f6f4 v[2:17], v[34:41], v[162:169], v[2:17], v234, v234 op_sel_hi:[0,0,0]
	s_waitcnt lgkmcnt(4)
	v_mfma_scale_f32_32x32x64_f8f6f4 v[2:17], v[26:33], v[170:177], v[2:17], v234, v234 op_sel_hi:[0,0,0]
	s_waitcnt lgkmcnt(2)
	v_mfma_scale_f32_32x32x64_f8f6f4 v[2:17], v[50:57], v[178:185], v[2:17], v234, v234 op_sel_hi:[0,0,0]
	s_waitcnt lgkmcnt(0)
	v_mfma_scale_f32_32x32x64_f8f6f4 v[2:17], v[42:49], v[186:193], v[2:17], v234, v234 op_sel_hi:[0,0,0]
	s_nop 15
	v_min3_f32 v146, v146, v147, v148
	v_min3_f32 v149, v149, v150, v151
	v_min3_f32 v152, v152, v153, v154
	v_min3_f32 v155, v155, v156, v157
	v_min3_f32 v158, v158, v159, v160
	v_min3_f32 v146, v146, v149, v152
	v_min3_f32 v155, v155, v158, v161
	v_min3_f32 v235, v235, v146, v155
	ds_bpermute_b32 v246, v232, v235
	s_waitcnt lgkmcnt(0)
	v_min_f32_e32 v246, v235, v246
	ds_write_b32 v233, v246 offset:49152
	ds_read_b128 v[146:149], v231 offset:34944
	ds_read_b128 v[150:153], v231 offset:34976
	ds_read_b128 v[154:157], v231 offset:35008
	ds_read_b128 v[158:161], v231 offset:35040
	s_waitcnt lgkmcnt(0)
	v_mfma_scale_f32_32x32x64_f8f6f4 v[146:161], v[18:25], v[162:169], v[146:161], v234, v234 op_sel_hi:[0,0,0]
	v_mfma_scale_f32_32x32x64_f8f6f4 v[146:161], v[130:137], v[170:177], v[146:161], v234, v234 op_sel_hi:[0,0,0]
	v_mfma_scale_f32_32x32x64_f8f6f4 v[146:161], v[122:129], v[178:185], v[146:161], v234, v234 op_sel_hi:[0,0,0]
	v_mfma_scale_f32_32x32x64_f8f6f4 v[146:161], v[138:145], v[186:193], v[146:161], v234, v234 op_sel_hi:[0,0,0]
	s_nop 15
	v_min3_f32 v2, v2, v3, v4
	v_min3_f32 v5, v5, v6, v7
	v_min3_f32 v8, v8, v9, v10
	v_min3_f32 v11, v11, v12, v13
	v_min3_f32 v14, v14, v15, v16
	v_min3_f32 v2, v2, v5, v8
	v_min3_f32 v11, v11, v14, v17
	v_min_f32_e32 v236, v2, v11
	ds_read_b128 v[2:5], v231 offset:35072
	ds_read_b128 v[6:9], v231 offset:35104
	ds_read_b128 v[10:13], v231 offset:35136
	ds_read_b128 v[14:17], v231 offset:35168
	s_waitcnt lgkmcnt(0)
	v_mfma_scale_f32_32x32x64_f8f6f4 v[2:17], v[98:105], v[162:169], v[2:17], v234, v234 op_sel_hi:[0,0,0]
	v_mfma_scale_f32_32x32x64_f8f6f4 v[2:17], v[90:97], v[170:177], v[2:17], v234, v234 op_sel_hi:[0,0,0]
	v_mfma_scale_f32_32x32x64_f8f6f4 v[2:17], v[114:121], v[178:185], v[2:17], v234, v234 op_sel_hi:[0,0,0]
	v_mfma_scale_f32_32x32x64_f8f6f4 v[2:17], v[106:113], v[186:193], v[2:17], v234, v234 op_sel_hi:[0,0,0]
	s_nop 15
	v_min3_f32 v146, v146, v147, v148
	v_min3_f32 v149, v149, v150, v151
	v_min3_f32 v152, v152, v153, v154
	v_min3_f32 v155, v155, v156, v157
	v_min3_f32 v158, v158, v159, v160
	v_min3_f32 v146, v146, v149, v152
	v_min3_f32 v155, v155, v158, v161
	v_min3_f32 v236, v236, v146, v155
	ds_read_b128 v[146:149], v231 offset:35200
	ds_read_b128 v[150:153], v231 offset:35232
	ds_read_b128 v[154:157], v231 offset:35264
	ds_read_b128 v[158:161], v231 offset:35296
	s_waitcnt lgkmcnt(0)
	v_mfma_scale_f32_32x32x64_f8f6f4 v[146:161], v[58:65], v[162:169], v[146:161], v234, v234 op_sel_hi:[0,0,0]
	v_mfma_scale_f32_32x32x64_f8f6f4 v[146:161], v[66:73], v[170:177], v[146:161], v234, v234 op_sel_hi:[0,0,0]
	v_mfma_scale_f32_32x32x64_f8f6f4 v[146:161], v[74:81], v[178:185], v[146:161], v234, v234 op_sel_hi:[0,0,0]
	v_mfma_scale_f32_32x32x64_f8f6f4 v[146:161], v[82:89], v[186:193], v[146:161], v234, v234 op_sel_hi:[0,0,0]
	s_nop 15
	v_min3_f32 v2, v2, v3, v4
	v_min3_f32 v5, v5, v6, v7
	v_min3_f32 v8, v8, v9, v10
	v_min3_f32 v11, v11, v12, v13
	v_min3_f32 v14, v14, v15, v16
	v_min3_f32 v2, v2, v5, v8
	v_min3_f32 v11, v11, v14, v17
	v_min3_f32 v236, v236, v2, v11
	s_nop 15
	s_nop 3
	v_min3_f32 v146, v146, v147, v148
	v_min3_f32 v149, v149, v150, v151
	v_min3_f32 v152, v152, v153, v154
	v_min3_f32 v155, v155, v156, v157
	v_min3_f32 v158, v158, v159, v160
	v_min3_f32 v146, v146, v149, v152
	v_min3_f32 v155, v155, v158, v161
	v_min3_f32 v236, v236, v146, v155
	ds_bpermute_b32 v246, v232, v236
	s_waitcnt lgkmcnt(0)
	v_min_f32_e32 v246, v236, v246
	ds_write_b32 v233, v246 offset:50176
	s_waitcnt lgkmcnt(0)
	s_barrier
	v_readfirstlane_b32 s2, v1
	s_nop 3
	s_cmp_gt_u32 s2, 1
	s_cbranch_scc1 .Lmain_idle
	v_and_b32_e32 v2, 31, v0
	v_lshlrev_b32_e32 v3, 5, v0
	v_and_b32_e32 v3, 0xc00, v3
	v_lshl_or_b32 v8, v2, 2, v3
	v_add_u32_e32 v8, 0xb800, v8
	v_lshlrev_b32_e32 v14, 6, v0
	ds_read2_b32 v[2:3], v8 offset1:32
	ds_read2_b32 v[4:5], v8 offset0:64 offset1:96
	ds_read2_b32 v[6:7], v8 offset0:128 offset1:160
	ds_read2_b32 v[10:11], v8 offset0:192 offset1:224
	ds_read_b128 v[20:23], v14 offset:38912
	ds_read_b128 v[24:27], v14 offset:38928
	ds_read_b128 v[28:31], v14 offset:38944
	ds_read_b128 v[32:35], v14 offset:38960
	s_mov_b32 s8, 0xf800000
	s_waitcnt lgkmcnt(4)
	v_min3_f32 v2, v2, v3, v4
	v_min3_f32 v5, v5, v6, v7
	v_min3_f32 v2, v2, v10, v11
	v_min_f32_e32 v2, v2, v5
	s_waitcnt lgkmcnt(0)
	v_add_f32_e32 v20, v20, v21
	v_add_f32_e32 v22, v22, v23
	v_add_f32_e32 v24, v24, v25
	v_add_f32_e32 v26, v26, v27
	v_add_f32_e32 v28, v28, v29
	v_add_f32_e32 v30, v30, v31
	v_add_f32_e32 v32, v32, v33
	v_add_f32_e32 v34, v34, v35
	v_add_f32_e32 v20, v20, v22
	v_add_f32_e32 v24, v24, v26
	v_add_f32_e32 v28, v28, v30
	v_add_f32_e32 v32, v32, v34
	v_add_f32_e32 v20, v20, v24
	v_add_f32_e32 v28, v28, v32
	v_add_f32_e32 v20, v20, v28
	v_add_f32_e32 v2, v2, v20
	v_max_f32_e32 v2, 0, v2
	v_mul_f32_e32 v3, 0x4f800000, v2
	v_cmp_gt_f32_e32 vcc, s8, v2
	s_nop 1
	v_cndmask_b32_e32 v2, v2, v3, vcc
	v_sqrt_f32_e32 v3, v2
	s_nop 0
	v_add_u32_e32 v4, -1, v3
	v_fma_f32 v5, -v4, v3, v2
	v_cmp_ge_f32_e64 s[10:11], 0, v5
	v_add_u32_e32 v5, 1, v3
	s_nop 0
	v_cndmask_b32_e64 v4, v3, v4, s[10:11]
	v_fma_f32 v3, -v5, v3, v2
	v_cmp_lt_f32_e64 s[10:11], 0, v3
	s_nop 1
	v_cndmask_b32_e64 v3, v4, v5, s[10:11]
	v_mul_f32_e32 v4, 0x37800000, v3
	v_cndmask_b32_e32 v3, v3, v4, vcc
	v_mov_b32_e32 v4, 0x260
	v_cmp_class_f32_e32 vcc, v2, v4
	s_nop 1
	v_cndmask_b32_e32 v2, v3, v2, vcc
	s_nop 1
	v_add_f32_dpp v3, v2, v2 quad_perm:[1,0,3,2] row_mask:0xf bank_mask:0xf
	s_nop 1
	v_add_f32_dpp v4, v3, v3 quad_perm:[2,3,0,1] row_mask:0xf bank_mask:0xf
	s_nop 1
	v_add_f32_dpp v5, v4, v4 row_half_mirror row_mask:0xf bank_mask:0xf
	s_nop 1
	v_add_f32_dpp v6, v5, v5 row_mirror row_mask:0xf bank_mask:0xf
	s_nop 1
	v_readlane_b32 s12, v6, 0
	v_readlane_b32 s13, v6, 16
	v_readlane_b32 s14, v6, 32
	v_readlane_b32 s15, v6, 48
	s_nop 3
	v_mov_b32_e32 v7, s12
	v_add_f32_e32 v7, s13, v7
	v_mov_b32_e32 v9, s14
	v_add_f32_e32 v9, s15, v9
	v_add_f32_e32 v7, v7, v9
	v_mov_b32_e32 v4, 0
	s_cmp_eq_u32 s2, 1
	s_cbranch_scc0 .Lmain_w0
	ds_write_b32 v4, v7 offset:51204
	s_waitcnt lgkmcnt(0)
